# sload
# speedup vs baseline: 1.0148x; 1.0148x over previous
.LBB0_23:
	s_and_b64 vcc, exec, s[4:5]
	s_cbranch_vccz .LBB0_358
	s_lshl_b32 s3, s2, 2
	s_addk_i32 s3, 0xf7a8
	v_lshrrev_b32_e32 v1, 6, v0
	v_or_b32_e32 v2, s3, v1
	s_load_dwordx4 s[12:15], s[0:1], 0x28
	s_load_dwordx2 s[4:5], s[0:1], 0x38
	s_load_dwordx2 s[24:25], s[0:1], 0x48
	v_ashrrev_i32_e32 v3, 31, v2
	v_and_b32_e32 v7, 63, v0
	v_lshlrev_b64 v[4:5], 7, v[2:3]
	v_or_b32_e32 v4, v4, v7
	v_lshlrev_b64 v[12:13], 2, v[4:5]
	s_waitcnt lgkmcnt(0)
	v_lshl_add_u64 v[8:9], s[12:13], 0, v[12:13]
	global_load_dword v10, v[8:9], off nt
	global_load_dword v11, v[8:9], off offset:256 nt
	v_lshl_add_u64 v[14:15], s[14:15], 0, v[12:13]
	v_lshl_add_u64 v[12:13], s[4:5], 0, v[12:13]
	global_load_dword v9, v[14:15], off nt
	global_load_dword v8, v[14:15], off offset:256 nt
	global_load_dword v1, v[12:13], off nt
	global_load_dword v6, v[12:13], off offset:256 nt
	s_mov_b32 s3, 0xbfb8aa3b
	s_waitcnt vmcnt(5)
	v_add_f32_e32 v10, 0xc1200000, v10
	v_mul_f32_e64 v12, |v10|, s3
	v_exp_f32_e32 v13, v12
	s_mov_b32 s3, 0x3c23d70a
	v_cmp_ngt_f32_e32 vcc, s3, v13
	s_and_saveexec_b64 s[4:5], vcc
	s_xor_b64 s[10:11], exec, s[4:5]
	s_cbranch_execz .LBB0_26
	v_add_f32_e32 v12, 1.0, v13
	s_mov_b32 s3, 0x800000
	v_cmp_gt_f32_e32 vcc, s3, v12
	s_mov_b32 s3, 0x3f317217
	s_nop 0
	v_cndmask_b32_e64 v13, 0, 32, vcc
	v_ldexp_f32 v12, v12, v13
	v_log_f32_e32 v12, v12
	s_nop 0
	v_mul_f32_e32 v13, 0x3f317217, v12
	v_fma_f32 v13, v12, s3, -v13
	v_fmamk_f32 v13, v12, 0x3377d1cf, v13
	s_mov_b32 s3, 0x7f800000
	v_fmac_f32_e32 v13, 0x3f317217, v12
	v_cmp_lt_f32_e64 s[4:5], |v12|, s3
	s_nop 1
	v_cndmask_b32_e64 v12, v12, v13, s[4:5]
	v_mov_b32_e32 v13, 0x41b17218
	v_cndmask_b32_e32 v13, 0, v13, vcc
	v_sub_f32_e32 v12, v12, v13

.LBB0_30:
	s_andn2_saveexec_b64 s[4:5], s[10:11]
	v_mov_b32_e32 v13, 0.5
	v_fmamk_f32 v13, v14, 0xbeaaaaab, v13
	v_fma_f32 v13, -v14, v13, 1.0
	v_mul_f32_e32 v13, v14, v13
	s_or_b64 exec, exec, s[4:5]
	v_max_f32_e32 v10, v10, v10
	v_max_f32_e32 v10, 0, v10
	v_add_f32_e32 v10, v10, v12
	s_waitcnt vmcnt(3)
	v_mul_f32_e32 v9, v9, v10
	v_mul_f32_e32 v10, 0x41c80000, v9
	s_mov_b32 s3, 0x3c23d70a
	v_cmp_ngt_f32_e32 vcc, s3, v10
	s_and_saveexec_b64 s[4:5], vcc
	s_xor_b64 s[4:5], exec, s[4:5]
	v_mul_f32_e32 v9, 0xbfb8aa3b, v10
	v_exp_f32_e32 v9, v9
	s_nop 0
	v_sub_f32_e32 v9, 1.0, v9
	s_andn2_saveexec_b64 s[4:5], s[4:5]
	v_mov_b32_e32 v9, 0.5
	v_fmamk_f32 v9, v10, 0xbe2aaaab, v9
	v_fma_f32 v9, -v10, v9, 1.0
	v_mul_f32_e32 v9, v10, v9
	s_or_b64 exec, exec, s[4:5]
	v_max_f32_e32 v10, v11, v11
	v_max_f32_e32 v10, 0, v10
	v_add_f32_e32 v10, v10, v13
	s_waitcnt vmcnt(2)
	v_mul_f32_e32 v8, v8, v10
	v_mul_f32_e32 v10, 0x41c80000, v8
	v_cmp_ngt_f32_e32 vcc, s3, v10
	s_and_saveexec_b64 s[4:5], vcc
	s_xor_b64 s[4:5], exec, s[4:5]
	v_mul_f32_e32 v8, 0xbfb8aa3b, v10
	v_exp_f32_e32 v8, v8
	s_nop 0
	v_sub_f32_e32 v8, 1.0, v8
	s_andn2_saveexec_b64 s[4:5], s[4:5]
	v_mov_b32_e32 v8, 0.5
	v_fmamk_f32 v8, v10, 0xbe2aaaab, v8
	v_fma_f32 v8, -v10, v8, 1.0
	v_mul_f32_e32 v8, v10, v8
	s_or_b64 exec, exec, s[4:5]
	v_cmp_eq_u32_e32 vcc, 63, v7
	v_mov_b32_e32 v12, 1.0
	v_mov_b32_e32 v11, 1.0
	v_cndmask_b32_e64 v7, v8, 1.0, vcc
	v_sub_f32_e32 v8, 1.0, v9
	v_add_f32_e32 v8, 0x2edbe6ff, v8
	v_sub_f32_e32 v10, 1.0, v7
	v_add_f32_e32 v10, 0x2edbe6ff, v10
	v_lshl_add_u64 v[4:5], v[4:5], 2, s[6:7]
	s_mov_b64 s[4:5], 0x216000
	v_mov_b32_e32 v12, 1.0
	v_mov_b32_e32 v64, 1.0
	v_mov_b32_dpp v12, v8 row_shr:1 row_mask:0xf bank_mask:0xf
	v_mov_b32_dpp v64, v10 row_shr:1 row_mask:0xf bank_mask:0xf
	v_mul_f32_e32 v8, v8, v12
	v_mul_f32_e32 v10, v10, v64
	v_mov_b32_e32 v12, 1.0
	v_mov_b32_e32 v64, 1.0
	v_mov_b32_dpp v12, v8 row_shr:2 row_mask:0xf bank_mask:0xf
	v_mov_b32_dpp v64, v10 row_shr:2 row_mask:0xf bank_mask:0xf
	v_mul_f32_e32 v8, v8, v12
	v_mul_f32_e32 v10, v10, v64
	v_mov_b32_e32 v12, 1.0
	v_mov_b32_e32 v64, 1.0
	v_mov_b32_dpp v12, v8 row_shr:4 row_mask:0xf bank_mask:0xf
	v_mov_b32_dpp v64, v10 row_shr:4 row_mask:0xf bank_mask:0xf
	v_mul_f32_e32 v8, v8, v12
	v_mul_f32_e32 v10, v10, v64
	v_mov_b32_e32 v12, 1.0
	v_mov_b32_e32 v64, 1.0
	v_mov_b32_dpp v12, v8 row_shr:8 row_mask:0xf bank_mask:0xf
	v_mov_b32_dpp v64, v10 row_shr:8 row_mask:0xf bank_mask:0xf
	v_mul_f32_e32 v8, v8, v12
	v_mul_f32_e32 v10, v10, v64
	v_mov_b32_e32 v12, 1.0
	v_mov_b32_e32 v64, 1.0
	v_mov_b32_dpp v12, v8 row_bcast:15 row_mask:0xa bank_mask:0xf
	v_mov_b32_dpp v64, v10 row_bcast:15 row_mask:0xa bank_mask:0xf
	v_mul_f32_e32 v8, v8, v12
	v_mul_f32_e32 v10, v10, v64
	v_mov_b32_e32 v12, 1.0
	v_mov_b32_e32 v64, 1.0
	v_mov_b32_dpp v12, v8 row_bcast:31 row_mask:0xc bank_mask:0xf
	v_mov_b32_dpp v64, v10 row_bcast:31 row_mask:0xc bank_mask:0xf
	v_mul_f32_e32 v8, v8, v12
	v_mul_f32_e32 v10, v10, v64
	v_mov_b32_e32 v12, 1.0
	v_mov_b32_e32 v64, 1.0
	v_readlane_b32 s3, v8, 63
	v_mov_b32_dpp v11, v10 wave_shr:1 row_mask:0xf bank_mask:0xf
	v_mov_b32_dpp v12, v8 wave_shr:1 row_mask:0xf bank_mask:0xf
	v_mul_f32_e32 v10, s3, v11
	s_mov_b32 s3, 0x216000
	v_mul_f32_e32 v13, v7, v10
	v_lshl_add_u64 v[10:11], v[4:5], 0, s[4:5]
	v_add_co_u32_e64 v4, s[4:5], s3, v4
	v_mul_f32_e32 v8, v9, v12
	s_nop 0
	v_addc_co_u32_e64 v5, s[4:5], 0, v5, s[4:5]
	s_waitcnt vmcnt(0)
	v_mul_f32_e32 v6, v6, v13
	global_store_dword v[4:5], v8, off
	global_store_dword v[10:11], v13, off offset:256
	v_fma_f32 v5, v9, v12, v13
	v_fmac_f32_e32 v6, v1, v8
	v_mov_b32_e32 v7, 0
	v_add_f32_dpp v5, v5, v5 row_shr:1 row_mask:0xf bank_mask:0xf bound_ctrl:1
	v_add_f32_dpp v1, v6, v6 row_shr:1 row_mask:0xf bank_mask:0xf bound_ctrl:1
	v_mov_b32_e32 v6, 0
	v_add_f32_dpp v5, v5, v5 row_shr:2 row_mask:0xf bank_mask:0xf bound_ctrl:1
	v_add_f32_dpp v1, v1, v1 row_shr:2 row_mask:0xf bank_mask:0xf bound_ctrl:1
	v_mov_b32_e32 v4, 0
	v_add_f32_dpp v5, v5, v5 row_shr:4 row_mask:0xf bank_mask:0xf bound_ctrl:1
	v_add_f32_dpp v1, v1, v1 row_shr:4 row_mask:0xf bank_mask:0xf bound_ctrl:1
	s_nop 0
	v_add_f32_dpp v5, v5, v5 row_shr:8 row_mask:0xf bank_mask:0xf bound_ctrl:1
	v_add_f32_dpp v1, v1, v1 row_shr:8 row_mask:0xf bank_mask:0xf bound_ctrl:1
	s_nop 0
	v_mov_b32_dpp v7, v5 row_bcast:15 row_mask:0xa bank_mask:0xf
	v_mov_b32_dpp v6, v1 row_bcast:15 row_mask:0xa bank_mask:0xf
	v_add_f32_e32 v5, v5, v7
	v_mov_b32_e32 v7, 0
	v_add_f32_e32 v1, v1, v6
	s_nop 0
	v_mov_b32_dpp v7, v5 row_bcast:31 row_mask:0xc bank_mask:0xf
	v_mov_b32_dpp v4, v1 row_bcast:31 row_mask:0xc bank_mask:0xf
	s_and_saveexec_b64 s[4:5], vcc
	s_cbranch_execz .LBB0_42
	v_add_f32_e32 v1, v1, v4
	v_add_f32_e32 v6, v5, v7
	s_waitcnt lgkmcnt(0)
	v_lshl_add_u64 v[2:3], v[2:3], 2, s[24:25]
	v_add_co_u32_e32 v4, vcc, 0xc000, v2
	s_nop 1
	v_addc_co_u32_e32 v5, vcc, 0, v3, vcc
	v_add_co_u32_e32 v2, vcc, 0x10000, v2
	global_store_dword v[4:5], v1, off
	s_nop 0
	v_addc_co_u32_e32 v3, vcc, 0, v3, vcc
	global_store_dword v[2:3], v6, off

	.amdhsa_kernel _Z11prep_kernelPKfS0_S0_S0_S0_S0_S0_S0_PhPf
		.amdhsa_group_segment_fixed_size 1280
		.amdhsa_private_segment_fixed_size 0
		.amdhsa_kernarg_size 80
		.amdhsa_user_sgpr_count 2
		.amdhsa_user_sgpr_dispatch_ptr 0
		.amdhsa_user_sgpr_queue_ptr 0
		.amdhsa_user_sgpr_kernarg_segment_ptr 1
		.amdhsa_user_sgpr_dispatch_id 0
		.amdhsa_user_sgpr_kernarg_preload_length 0
		.amdhsa_user_sgpr_kernarg_preload_offset 0
		.amdhsa_user_sgpr_private_segment_size 0
		.amdhsa_uses_dynamic_stack 0
		.amdhsa_enable_private_segment 0
		.amdhsa_system_sgpr_workgroup_id_x 1
		.amdhsa_system_sgpr_workgroup_id_y 0
		.amdhsa_system_sgpr_workgroup_id_z 0
		.amdhsa_system_sgpr_workgroup_info 0
		.amdhsa_system_vgpr_workitem_id 0
		.amdhsa_next_free_vgpr 72
		.amdhsa_next_free_sgpr 26
		.amdhsa_accum_offset 72
		.amdhsa_reserve_vcc 1
		.amdhsa_float_round_mode_32 0
		.amdhsa_float_round_mode_16_64 0
		.amdhsa_float_denorm_mode_32 3
		.amdhsa_float_denorm_mode_16_64 3
		.amdhsa_dx10_clamp 1
		.amdhsa_ieee_mode 1
		.amdhsa_fp16_overflow 0
		.amdhsa_tg_split 0
		.amdhsa_exception_fp_ieee_invalid_op 0
		.amdhsa_exception_fp_denorm_src 0
		.amdhsa_exception_fp_ieee_div_zero 0
		.amdhsa_exception_fp_ieee_overflow 0
		.amdhsa_exception_fp_ieee_underflow 0
		.amdhsa_exception_fp_ieee_inexact 0
		.amdhsa_exception_int_div_zero 0
	.end_amdhsa_kernel

amdhsa.kernels:
  - .agpr_count:     0
    .args:
      - .actual_access:  read_only
        .address_space:  global
        .offset:         0
        .size:           8
        .value_kind:     global_buffer
      - .actual_access:  read_only
        .address_space:  global
        .offset:         8
        .size:           8
        .value_kind:     global_buffer
      - .actual_access:  read_only
        .address_space:  global
        .offset:         16
        .size:           8
        .value_kind:     global_buffer
      - .actual_access:  read_only
        .address_space:  global
        .offset:         24
        .size:           8
        .value_kind:     global_buffer
      - .actual_access:  read_only
        .address_space:  global
        .offset:         32
        .size:           8
        .value_kind:     global_buffer
      - .actual_access:  read_only
        .address_space:  global
        .offset:         40
        .size:           8
        .value_kind:     global_buffer
      - .actual_access:  read_only
        .address_space:  global
        .offset:         48
        .size:           8
        .value_kind:     global_buffer
      - .actual_access:  read_only
        .address_space:  global
        .offset:         56
        .size:           8
        .value_kind:     global_buffer
      - .actual_access:  write_only
        .address_space:  global
        .offset:         64
        .size:           8
        .value_kind:     global_buffer
      - .actual_access:  write_only
        .address_space:  global
        .offset:         72
        .size:           8
        .value_kind:     global_buffer
    .group_segment_fixed_size: 1280
    .kernarg_segment_align: 8
    .kernarg_segment_size: 80
    .language:       OpenCL C
    .language_version:
      - 2
      - 0
    .max_flat_workgroup_size: 256
    .name:           _Z11prep_kernelPKfS0_S0_S0_S0_S0_S0_S0_PhPf
    .private_segment_fixed_size: 0
    .sgpr_count:     32
    .sgpr_spill_count: 0
    .symbol:         _Z11prep_kernelPKfS0_S0_S0_S0_S0_S0_S0_PhPf.kd
    .uniform_work_group_size: 1
    .uses_dynamic_stack: false
    .vgpr_count:     72
    .vgpr_spill_count: 0
    .wavefront_size: 64
  - .agpr_count:     0
    .args:
      - .actual_access:  read_only
        .address_space:  global
        .offset:         0
        .size:           8
        .value_kind:     global_buffer
      - .address_space:  global
        .offset:         8
        .size:           8
        .value_kind:     global_buffer
      - .actual_access:  read_only
        .address_space:  global
        .offset:         16
        .size:           8
        .value_kind:     global_buffer
      - .actual_access:  read_only
        .address_space:  global
        .offset:         24
        .size:           8
        .value_kind:     global_buffer
      - .actual_access:  write_only
        .address_space:  global
        .offset:         32
        .size:           8
        .value_kind:     global_buffer
    .group_segment_fixed_size: 0
    .kernarg_segment_align: 8
    .kernarg_segment_size: 40
    .language:       OpenCL C
    .language_version:
      - 2
      - 0
    .max_flat_workgroup_size: 512
    .name:           _Z13render_kernelPKfPKhS0_S0_Pf
    .private_segment_fixed_size: 0
    .sgpr_count:     28
    .sgpr_spill_count: 0
    .symbol:         _Z13render_kernelPKfPKhS0_S0_Pf.kd
    .uniform_work_group_size: 1
    .uses_dynamic_stack: false
    .vgpr_count:     256
    .vgpr_spill_count: 0
    .wavefront_size: 64
